# move weight-conversion part D (F2 tiles) from norm1 into FFN1 unit epilogues: per-wave dword loads issued mid-epilogue, converted and stored at epilogue end (no LDS transpose)
# speedup vs baseline: 1.0071x; 1.0071x over previous
.LBB0_255:
	s_or_b64 exec, exec, s[10:11]
	s_add_i32 s3, s3, 1
	s_cmp_lg_u32 s3, 3
	s_cbranch_scc0 .LBB0_324

.LBB0_1908:
	v_readlane_b32 s78, v254, 2
	v_readlane_b32 s79, v254, 3
	v_readlane_b32 s72, v254, 10
	v_lshrrev_b32_e32 v2, 6, v0
	s_nop 4
	s_load_dwordx2 s[80:81], s[78:79], 0x100
	s_load_dwordx2 s[78:79], s[78:79], 0x118
	v_readfirstlane_b32 s32, v2
	s_waitcnt lgkmcnt(0)
	s_lshl_b32 s72, s72, 27
	s_add_u32 s80, s80, s72
	s_addc_u32 s81, s81, 0
	s_lshl_b32 s72, s32, 15
	s_add_u32 s80, s80, s72
	s_addc_u32 s81, s81, 0
	s_add_u32 s78, s78, 0x9bb0000
	s_addc_u32 s79, s79, 0
	s_lshl_b32 s72, s32, 3
	s_add_u32 s78, s78, s72
	s_addc_u32 s79, s79, 0
	v_writelane_b32 v255, s80, 40
	v_writelane_b32 v255, s81, 41
	v_writelane_b32 v255, s78, 42
	v_writelane_b32 v255, s79, 43
	s_mov_b32 s32, 0
	v_readlane_b32 s8, v255, 3
	v_readlane_b32 s9, v255, 4
	s_and_b64 s[8:9], s[8:9], exec
	v_readlane_b32 s0, v254, 2
	s_cselect_b32 s3, 16, 17
	v_readlane_b32 s1, v254, 3
	v_mov_b32_e32 v2, v0
	s_lshl_b32 s8, s3, 8
	s_mov_b32 s6, s2
	s_cmp_ge_i32 s6, s8
	v_readfirstlane_b32 s10, v2
	s_cbranch_scc1 .LBB0_1922
	s_waitcnt vmcnt(0)
	v_ashrrev_i32_e32 v5, 31, v2
	v_lshrrev_b32_e32 v5, 26, v5
	v_add_u32_e32 v5, v2, v5
	v_ashrrev_i32_e32 v12, 6, v5
	v_bfe_i32 v5, v2, 27, 1
	v_lshlrev_b32_e32 v4, 4, v2
	v_lshrrev_b32_e32 v5, 22, v5
	v_add_u32_e32 v5, v4, v5
	v_and_b32_e32 v5, 0xfffffc00, v5
	v_sub_u32_e32 v5, v4, v5
	v_lshrrev_b32_e32 v6, 4, v5
	s_load_dwordx2 s[38:39], s[0:1], 0x118
	v_bitop3_b32 v13, v6, v5, 32 bitop3:0x6c
	v_ashrrev_i32_e32 v5, 31, v5
	v_lshrrev_b32_e32 v5, 26, v5
	v_add_u32_e32 v5, v13, v5
	v_add_u32_e32 v4, 0x2000, v4
	v_ashrrev_i32_e32 v14, 6, v5
	v_ashrrev_i32_e32 v5, 31, v4
	v_lshrrev_b32_e32 v5, 22, v5
	s_waitcnt lgkmcnt(0)
	s_add_u32 s26, s38, 0x163b0000
	v_add_u32_e32 v5, v4, v5
	s_addc_u32 s27, s39, 0
	v_ashrrev_i32_e32 v15, 10, v5
	s_add_u32 s11, s38, 0x1bb0000
	v_mul_i32_i24_e32 v5, 0x400, v15
	s_addc_u32 s12, s39, 0
	v_sub_u32_e32 v4, v4, v5
	s_add_u32 s21, s38, 0x233f0000
	v_lshrrev_b32_e32 v5, 4, v4
	s_addc_u32 s25, s39, 0
	v_bitop3_b32 v16, v5, v4, 32 bitop3:0x6c
	v_lshlrev_b32_e32 v5, 3, v12
	s_lshl_b32 s59, s3, 4
	v_and_b32_e32 v5, -16, v5
	s_abs_i32 s60, s59
	v_add_u32_e32 v6, v14, v5
	v_cvt_f32_u32_e32 v5, s60
	s_ashr_i32 s9, s6, 31
	s_lshr_b32 s9, s9, 29
	s_add_i32 s9, s6, s9
	v_rcp_iflag_f32_e32 v5, v5
	s_ashr_i32 s36, s9, 3
	s_and_b32 s9, s9, -8
	s_sub_i32 s6, s6, s9
	v_mul_f32_e32 v5, 0x4f7ffffe, v5
	v_cvt_u32_f32_e32 v5, v5
	s_lshl_b32 s58, s3, 5
	s_lshr_b32 s9, s6, 31
	s_or_b32 s9, s9, s58
	s_mul_i32 s6, s9, s6
	s_add_i32 s6, s6, s36
	s_sub_i32 s36, 0, s60
	v_readfirstlane_b32 s62, v5
	s_mul_i32 s36, s36, s62
	s_ashr_i32 s9, s6, 31
	s_bfe_i32 s61, s3, 0x1001b
	s_mul_hi_u32 s36, s62, s36
	s_xor_b32 s3, s9, s61
	s_abs_i32 s9, s6
	s_add_i32 s62, s62, s36
	s_mul_hi_u32 s36, s9, s62
	s_mul_i32 s37, s36, s60
	s_ashr_i32 s1, s10, 6
	s_sub_i32 s9, s9, s37
	s_ashr_i32 s0, s10, 8
	s_lshl_b32 s56, s1, 10
	s_add_i32 s37, s36, 1
	s_sub_i32 s40, s9, s60
	s_cmp_ge_u32 s9, s60
	s_cselect_b32 s36, s37, s36
	s_cselect_b32 s9, s40, s9
	s_add_i32 s37, s36, 1
	s_cmp_ge_u32 s9, s60
	s_cselect_b32 s9, s37, s36
	s_xor_b32 s9, s9, s3
	s_sub_i32 s40, s9, s3
	s_mul_i32 s3, s40, s59
	s_sub_i32 s3, s6, s3
	s_bfe_u32 s9, s3, 0x4001b
	s_add_i32 s9, s3, s9
	s_sext_i32_i16 s36, s9
	v_ashrrev_i32_e32 v4, 31, v16
	s_mul_i32 s6, s40, 17
	s_ashr_i32 s36, s36, 4
	v_lshrrev_b32_e32 v4, 26, v4
	s_add_i32 s48, s6, s36
	v_add_u32_e32 v17, v16, v4
	v_lshlrev_b32_e32 v4, 3, v15
	s_and_b32 s6, s9, 0xfff0
	s_ashr_i32 s49, s48, 31
	v_ashrrev_i32_e32 v18, 6, v17
	v_and_b32_e32 v4, -16, v4
	s_sub_i32 s42, s3, s6
	s_lshl_b64 s[36:37], s[48:49], 10
	v_add_u32_e32 v4, v18, v4
	s_add_u32 s36, s21, s36
	s_addc_u32 s37, s25, s37
	v_ashrrev_i32_e32 v7, 31, v6
	v_ashrrev_i32_e32 v5, 31, v4
	v_mov_b32_e32 v117, 0x7a7a7a7a
	v_mov_b32_e32 v198, 0x7f7f7f7f
	v_lshl_add_u64 v[8:9], v[6:7], 2, s[36:37]
	v_lshl_add_u64 v[10:11], v[4:5], 2, s[36:37]
	s_load_dword s57, s[96:97], 0x0
	global_load_dword v19, v[8:9], off
	global_load_dword v20, v[10:11], off
	s_nop 0
	global_load_dword v10, v[10:11], off offset:512
	s_nop 0
	global_load_dword v8, v[8:9], off offset:512
	v_mul_i32_i24_e32 v11, 64, v14
	v_sub_u32_e32 v11, v13, v11
	v_lshlrev_b32_e32 v9, 5, v12
	v_ashrrev_i16_sdwa v11, v250, sext(v11) dst_sel:DWORD dst_unused:UNUSED_PAD src0_sel:DWORD src1_sel:BYTE_0
	v_and_b32_e32 v9, 32, v9
	v_bfe_i32 v11, v11, 0, 16
	v_add_lshl_u32 v199, v9, v11, 1
	v_and_b32_e32 v11, 0xc0, v17
	v_sub_u32_e32 v11, v16, v11
	v_lshlrev_b32_e32 v9, 5, v15
	v_ashrrev_i16_sdwa v11, v250, sext(v11) dst_sel:DWORD dst_unused:UNUSED_PAD src0_sel:DWORD src1_sel:BYTE_0
	v_and_b32_e32 v9, 32, v9
	v_bfe_i32 v11, v11, 0, 16
	v_add_lshl_u32 v200, v9, v11, 1
	v_and_b32_e32 v9, 3, v18
	s_mov_b32 s3, 0x3fffe0
	v_lshrrev_b32_e32 v11, 2, v4
	v_lshlrev_b32_e32 v12, 1, v4
	v_and_or_b32 v9, v4, s3, v9
	v_and_b32_e32 v11, 4, v11
	v_and_b32_e32 v12, 24, v12
	v_or3_b32 v9, v9, v11, v12
	s_ashr_i32 s41, s40, 31
	v_lshl_add_u32 v166, v9, 10, v200
	v_and_b32_e32 v9, 3, v14
	s_lshl_b64 s[40:41], s[40:41], 22
	v_and_or_b32 v9, v6, s3, v9
	s_add_u32 s3, s11, s40
	s_addc_u32 s6, s12, s41
	s_bfe_i64 s[40:41], s[42:43], 0x100000
	v_lshrrev_b32_e32 v11, 2, v6
	v_lshlrev_b32_e32 v12, 1, v6
	s_lshl_b64 s[40:41], s[40:41], 18
	v_and_b32_e32 v11, 4, v11
	v_and_b32_e32 v12, 24, v12
	s_add_u32 s50, s3, s40
	v_or3_b32 v9, v9, v11, v12
	s_addc_u32 s51, s6, s41
	s_add_i32 s49, s56, 0
	v_lshl_add_u32 v168, v9, 10, v199
	s_add_i32 m0, s49, 0x10400
	s_add_i32 s63, s49, 0x400
	global_load_lds_dwordx4 v168, s[50:51]
	s_add_i32 m0, s49, 0x12400
	s_add_i32 s64, s49, 0x2400
	global_load_lds_dwordx4 v166, s[50:51]
	s_mov_b32 m0, s63
	s_add_u32 s40, s50, 0x20000
	s_addc_u32 s41, s51, 0
	s_add_i32 s65, s49, 0x4400
	s_add_i32 s66, s49, 0x6400
	v_mov_b32_e32 v169, v3
	v_mov_b32_e32 v167, v3
	v_mov_b32_e32 v185, v3
	v_mov_b32_e32 v181, v3
	v_lshl_add_u64 v[14:15], s[50:51], 0, v[168:169]
	v_lshl_add_u64 v[12:13], s[50:51], 0, v[166:167]
	s_waitcnt vmcnt(0)
	v_lshl_add_u32 v184, v19, 10, v199
	v_lshl_add_u32 v180, v20, 10, v200
	global_load_lds_dwordx4 v184, s[26:27]
	s_mov_b32 m0, s64
	v_lshl_add_u32 v178, v8, 10, v199
	global_load_lds_dwordx4 v180, s[26:27]
	s_add_i32 m0, s49, 0x14400
	v_lshl_add_u32 v176, v10, 10, v200
	global_load_lds_dwordx4 v168, s[40:41]
	s_add_i32 m0, s49, 0x16400
	v_lshl_add_u64 v[10:11], s[26:27], 0, v[184:185]
	global_load_lds_dwordx4 v166, s[40:41]
	s_mov_b32 m0, s65
	s_cmp_lg_u32 s0, 1
	global_load_lds_dwordx4 v178, s[26:27]
	s_mov_b32 m0, s66
	v_lshl_add_u64 v[8:9], s[26:27], 0, v[180:181]
	global_load_lds_dwordx4 v176, s[26:27]
	s_cbranch_scc1 .LBB0_1911
	s_barrier

.LBB0_1912:
	v_mul_f32_e32 v2, 0xbfb8aa3b, v162
	v_mul_f32_e32 v6, 0xbfb8aa3b, v163
	v_exp_f32_e32 v2, v2
	v_exp_f32_e32 v6, v6
	v_mul_f32_e32 v7, 0xbfb8aa3b, v164
	v_mul_f32_e32 v8, 0xbfb8aa3b, v165
	v_add_f32_e32 v2, 1.0, v2
	v_add_f32_e32 v6, 1.0, v6
	v_exp_f32_e32 v7, v7
	v_exp_f32_e32 v8, v8
	v_mul_f32_e32 v9, 0xbfb8aa3b, v154
	v_mul_f32_e32 v10, 0xbfb8aa3b, v155
	v_rcp_f32_e32 v2, v2
	v_rcp_f32_e32 v6, v6
	v_exp_f32_e32 v9, v9
	v_exp_f32_e32 v10, v10
	v_add_f32_e32 v7, 1.0, v7
	v_add_f32_e32 v8, 1.0, v8
	v_mul_f32_e32 v11, 0xbfb8aa3b, v156
	v_mul_f32_e32 v12, 0xbfb8aa3b, v157
	v_mul_f32_e32 v2, v162, v2
	v_mul_f32_e32 v6, v163, v6
	v_rcp_f32_e32 v7, v7
	v_rcp_f32_e32 v8, v8
	v_add_f32_e32 v9, 1.0, v9
	v_add_f32_e32 v10, 1.0, v10
	v_exp_f32_e32 v11, v11
	v_exp_f32_e32 v12, v12
	v_mul_f32_e32 v2, v2, v158
	v_mul_f32_e32 v6, v6, v159
	v_rcp_f32_e32 v9, v9
	v_rcp_f32_e32 v10, v10
	v_med3_f32 v2, v2, s7, v228
	v_med3_f32 v13, v6, s7, v228
	v_mov_b32_e32 v6, v3
	v_cvt_pk_fp8_f32 v6, v2, v13
	v_mul_f32_e32 v7, v164, v7
	v_mul_f32_e32 v8, v165, v8
	v_add_f32_e32 v11, 1.0, v11
	v_add_f32_e32 v12, 1.0, v12
	v_mul_f32_e32 v7, v7, v160
	v_mul_f32_e32 v8, v8, v161
	v_mul_f32_e32 v9, v154, v9
	v_mul_f32_e32 v10, v155, v10
	v_rcp_f32_e32 v11, v11
	v_rcp_f32_e32 v12, v12
	v_mul_f32_e32 v9, v9, v150
	v_mul_f32_e32 v10, v10, v151
	v_med3_f32 v2, v7, s7, v228
	v_med3_f32 v7, v8, s7, v228
	v_cvt_pk_fp8_f32 v6, v2, v7 op_sel:[0,0,1]
	v_med3_f32 v2, v9, s7, v228
	v_med3_f32 v8, v10, s7, v228
	v_mov_b32_e32 v7, v3
	v_cvt_pk_fp8_f32 v7, v2, v8
	v_lshl_add_u32 v4, s48, 8, v181
	v_mul_f32_e32 v11, v156, v11
	v_mul_f32_e32 v12, v157, v12
	v_ashrrev_i32_e32 v5, 31, v4
	v_mul_f32_e32 v11, v11, v152
	v_mul_f32_e32 v12, v12, v153
	v_lshlrev_b64 v[4:5], 11, v[4:5]
	s_lshl_b32 s0, s3, 7
	v_med3_f32 v2, v11, s7, v228
	v_med3_f32 v8, v12, s7, v228
	v_lshl_add_u64 v[4:5], s[40:41], 0, v[4:5]
	s_ashr_i32 s1, s0, 31
	v_cvt_pk_fp8_f32 v7, v2, v8 op_sel:[0,0,1]
	v_lshl_add_u64 v[4:5], v[4:5], 0, s[0:1]
	v_lshl_add_u64 v[4:5], v[4:5], 0, s[76:77]
	v_lshl_add_u64 v[4:5], v[4:5], 0, v[170:171]
	s_nop 15
	s_nop 15
	global_store_dwordx2 v[4:5], v[6:7], off
	v_mul_f32_e32 v2, 0xbfb8aa3b, v146
	v_mul_f32_e32 v6, 0xbfb8aa3b, v147
	v_exp_f32_e32 v2, v2
	v_exp_f32_e32 v6, v6
	v_mul_f32_e32 v7, 0xbfb8aa3b, v148
	v_mul_f32_e32 v8, 0xbfb8aa3b, v149
	v_add_f32_e32 v2, 1.0, v2
	v_add_f32_e32 v6, 1.0, v6
	v_exp_f32_e32 v7, v7
	v_exp_f32_e32 v8, v8
	v_mul_f32_e32 v9, 0xbfb8aa3b, v138
	v_mul_f32_e32 v10, 0xbfb8aa3b, v139
	v_rcp_f32_e32 v2, v2
	v_rcp_f32_e32 v6, v6
	v_exp_f32_e32 v9, v9
	v_exp_f32_e32 v10, v10
	v_add_f32_e32 v7, 1.0, v7
	v_add_f32_e32 v8, 1.0, v8
	v_mul_f32_e32 v11, 0xbfb8aa3b, v140
	v_mul_f32_e32 v12, 0xbfb8aa3b, v141
	v_mul_f32_e32 v2, v146, v2
	v_mul_f32_e32 v6, v147, v6
	v_rcp_f32_e32 v7, v7
	v_rcp_f32_e32 v8, v8
	v_add_f32_e32 v9, 1.0, v9
	v_add_f32_e32 v10, 1.0, v10
	v_exp_f32_e32 v11, v11
	v_exp_f32_e32 v12, v12
	v_mul_f32_e32 v2, v2, v142
	v_mul_f32_e32 v6, v6, v143
	v_rcp_f32_e32 v9, v9
	v_rcp_f32_e32 v10, v10
	v_med3_f32 v2, v2, s7, v228
	v_med3_f32 v13, v6, s7, v228
	v_mov_b32_e32 v6, v3
	v_cvt_pk_fp8_f32 v6, v2, v13
	v_mul_f32_e32 v7, v148, v7
	v_mul_f32_e32 v8, v149, v8
	v_add_f32_e32 v11, 1.0, v11
	v_add_f32_e32 v12, 1.0, v12
	v_mul_f32_e32 v7, v7, v144
	v_mul_f32_e32 v8, v8, v145
	v_mul_f32_e32 v9, v138, v9
	v_mul_f32_e32 v10, v139, v10
	v_rcp_f32_e32 v11, v11
	v_rcp_f32_e32 v12, v12
	v_mul_f32_e32 v9, v9, v134
	v_mul_f32_e32 v10, v10, v135
	v_med3_f32 v2, v7, s7, v228
	v_med3_f32 v7, v8, s7, v228
	v_cvt_pk_fp8_f32 v6, v2, v7 op_sel:[0,0,1]
	v_med3_f32 v2, v9, s7, v228
	v_med3_f32 v8, v10, s7, v228
	v_mov_b32_e32 v7, v3
	v_cvt_pk_fp8_f32 v7, v2, v8
	v_mul_f32_e32 v11, v140, v11
	v_mul_f32_e32 v12, v141, v12
	v_mul_f32_e32 v11, v11, v136
	v_mul_f32_e32 v12, v12, v137
	v_med3_f32 v2, v11, s7, v228
	v_med3_f32 v8, v12, s7, v228
	v_cvt_pk_fp8_f32 v7, v2, v8 op_sel:[0,0,1]
	v_add_co_u32_e32 v8, vcc, s31, v4
	v_mul_f32_e32 v2, 0xbfb8aa3b, v130
	s_nop 0
	v_addc_co_u32_e32 v9, vcc, 0, v5, vcc
	global_store_dwordx2 v[8:9], v[6:7], off
	s_lshl_b32 s72, s32, 8
	s_add_i32 s72, s72, s2
	s_cmpk_ge_i32 s72, 7136
	s_cbranch_scc1 .Lcvd_p1_end
	v_readlane_b32 s78, v255, 40
	v_readlane_b32 s79, v255, 41
	s_addk_i32 s72, 1056
	s_lshr_b32 s80, s72, 4
	s_lshl_b32 s80, s80, 18
	s_and_b32 s81, s72, 15
	s_lshl_b32 s81, s81, 8
	s_add_i32 s80, s80, s81
	v_and_b32_e32 v150, 63, v0
	v_lshl_add_u32 v150, v150, 2, s80
	v_add_u32_e32 v135, 0x1000, v150
	v_add_u32_e32 v136, 0x2000, v150
	v_add_u32_e32 v137, 0x3000, v150
	v_add_u32_e32 v138, 0x4000, v150
	v_add_u32_e32 v139, 0x5000, v150
	v_add_u32_e32 v140, 0x6000, v150
	v_add_u32_e32 v141, 0x7000, v150
	global_load_dword v134, v150, s[78:79]
	global_load_dword v135, v135, s[78:79]
	global_load_dword v136, v136, s[78:79]
	global_load_dword v137, v137, s[78:79]
	global_load_dword v138, v138, s[78:79]
	global_load_dword v139, v139, s[78:79]
	global_load_dword v140, v140, s[78:79]
	global_load_dword v141, v141, s[78:79]
	s_cmpk_ge_i32 s72, 7936
	s_cbranch_scc1 .Lcvd_p1_end
	v_add_u32_e32 v142, 0x400000, v150
	v_add_u32_e32 v143, 0x401000, v150
	v_add_u32_e32 v144, 0x402000, v150
	v_add_u32_e32 v145, 0x403000, v150
	v_add_u32_e32 v146, 0x404000, v150
	v_add_u32_e32 v147, 0x405000, v150
	v_add_u32_e32 v148, 0x406000, v150
	v_add_u32_e32 v149, 0x407000, v150
	global_load_dword v142, v142, s[78:79]
	global_load_dword v143, v143, s[78:79]
	global_load_dword v144, v144, s[78:79]
	global_load_dword v145, v145, s[78:79]
	global_load_dword v146, v146, s[78:79]
	global_load_dword v147, v147, s[78:79]
	global_load_dword v148, v148, s[78:79]
	global_load_dword v149, v149, s[78:79]
.Lcvd_p1_end:
	v_mul_f32_e32 v6, 0xbfb8aa3b, v131
	v_exp_f32_e32 v2, v2
	v_exp_f32_e32 v6, v6
	v_mul_f32_e32 v7, 0xbfb8aa3b, v132
	v_mul_f32_e32 v8, 0xbfb8aa3b, v133
	v_add_f32_e32 v2, 1.0, v2
	v_add_f32_e32 v6, 1.0, v6
	v_exp_f32_e32 v7, v7
	v_exp_f32_e32 v8, v8
	v_mul_f32_e32 v9, 0xbfb8aa3b, v122
	v_mul_f32_e32 v10, 0xbfb8aa3b, v123
	v_rcp_f32_e32 v2, v2
	v_rcp_f32_e32 v6, v6
	v_exp_f32_e32 v9, v9
	v_exp_f32_e32 v10, v10
	v_add_f32_e32 v7, 1.0, v7
	v_add_f32_e32 v8, 1.0, v8
	v_mul_f32_e32 v11, 0xbfb8aa3b, v124
	v_mul_f32_e32 v12, 0xbfb8aa3b, v125
	v_mul_f32_e32 v2, v130, v2
	v_mul_f32_e32 v6, v131, v6
	v_rcp_f32_e32 v7, v7
	v_rcp_f32_e32 v8, v8
	v_add_f32_e32 v9, 1.0, v9
	v_add_f32_e32 v10, 1.0, v10
	v_exp_f32_e32 v11, v11
	v_exp_f32_e32 v12, v12
	v_mul_f32_e32 v2, v2, v126
	v_mul_f32_e32 v6, v6, v127
	v_rcp_f32_e32 v9, v9
	v_rcp_f32_e32 v10, v10
	v_med3_f32 v2, v2, s7, v228
	v_med3_f32 v13, v6, s7, v228
	v_mov_b32_e32 v6, v3
	v_cvt_pk_fp8_f32 v6, v2, v13
	v_mul_f32_e32 v7, v132, v7
	v_mul_f32_e32 v8, v133, v8
	v_add_f32_e32 v11, 1.0, v11
	v_add_f32_e32 v12, 1.0, v12
	v_mul_f32_e32 v7, v7, v128
	v_mul_f32_e32 v8, v8, v129
	v_mul_f32_e32 v9, v122, v9
	v_mul_f32_e32 v10, v123, v10
	v_rcp_f32_e32 v11, v11
	v_rcp_f32_e32 v12, v12
	v_mul_f32_e32 v9, v9, v118
	v_mul_f32_e32 v10, v10, v119
	v_med3_f32 v2, v7, s7, v228
	v_med3_f32 v7, v8, s7, v228
	v_cvt_pk_fp8_f32 v6, v2, v7 op_sel:[0,0,1]
	v_med3_f32 v2, v9, s7, v228
	v_med3_f32 v8, v10, s7, v228
	v_mov_b32_e32 v7, v3
	v_cvt_pk_fp8_f32 v7, v2, v8
	v_mul_f32_e32 v11, v124, v11
	v_mul_f32_e32 v12, v125, v12
	v_mul_f32_e32 v11, v11, v120
	v_mul_f32_e32 v12, v12, v121
	v_med3_f32 v2, v11, s7, v228
	v_med3_f32 v8, v12, s7, v228
	v_cvt_pk_fp8_f32 v7, v2, v8 op_sel:[0,0,1]
	s_mov_b32 s0, 0x10000
	v_add_co_u32_e32 v8, vcc, s0, v4
	v_mul_f32_e32 v2, 0xbfb8aa3b, v112
	s_nop 0
	v_addc_co_u32_e32 v9, vcc, 0, v5, vcc
	global_store_dwordx2 v[8:9], v[6:7], off
	v_mul_f32_e32 v6, 0xbfb8aa3b, v113
	v_exp_f32_e32 v2, v2
	v_exp_f32_e32 v6, v6
	v_mul_f32_e32 v7, 0xbfb8aa3b, v114
	v_mul_f32_e32 v8, 0xbfb8aa3b, v115
	v_add_f32_e32 v2, 1.0, v2
	v_add_f32_e32 v6, 1.0, v6
	v_exp_f32_e32 v7, v7
	v_exp_f32_e32 v8, v8
	v_mul_f32_e32 v9, 0xbfb8aa3b, v104
	v_mul_f32_e32 v10, 0xbfb8aa3b, v105
	v_rcp_f32_e32 v2, v2
	v_rcp_f32_e32 v6, v6
	v_exp_f32_e32 v9, v9
	v_exp_f32_e32 v10, v10
	v_add_f32_e32 v7, 1.0, v7
	v_add_f32_e32 v8, 1.0, v8
	v_mul_f32_e32 v11, 0xbfb8aa3b, v106
	v_mul_f32_e32 v12, 0xbfb8aa3b, v107
	v_mul_f32_e32 v2, v112, v2
	v_mul_f32_e32 v6, v113, v6
	v_rcp_f32_e32 v7, v7
	v_rcp_f32_e32 v8, v8
	v_add_f32_e32 v9, 1.0, v9
	v_add_f32_e32 v10, 1.0, v10
	v_exp_f32_e32 v11, v11
	v_exp_f32_e32 v12, v12
	v_mul_f32_e32 v2, v2, v108
	v_mul_f32_e32 v6, v6, v109
	v_rcp_f32_e32 v9, v9
	v_rcp_f32_e32 v10, v10
	v_med3_f32 v2, v2, s7, v228
	v_med3_f32 v13, v6, s7, v228
	v_mov_b32_e32 v6, v3
	v_cvt_pk_fp8_f32 v6, v2, v13
	v_mul_f32_e32 v7, v114, v7
	v_mul_f32_e32 v8, v115, v8
	v_add_f32_e32 v11, 1.0, v11
	v_add_f32_e32 v12, 1.0, v12
	v_mul_f32_e32 v7, v7, v110
	v_mul_f32_e32 v8, v8, v111
	v_mul_f32_e32 v9, v104, v9
	v_mul_f32_e32 v10, v105, v10
	v_rcp_f32_e32 v11, v11
	v_rcp_f32_e32 v12, v12
	v_mul_f32_e32 v9, v9, v100
	v_mul_f32_e32 v10, v10, v101
	v_med3_f32 v2, v7, s7, v228
	v_med3_f32 v7, v8, s7, v228
	v_cvt_pk_fp8_f32 v6, v2, v7 op_sel:[0,0,1]
	v_med3_f32 v2, v9, s7, v228
	v_med3_f32 v8, v10, s7, v228
	v_mov_b32_e32 v7, v3
	v_cvt_pk_fp8_f32 v7, v2, v8
	v_mul_f32_e32 v11, v106, v11
	v_mul_f32_e32 v12, v107, v12
	v_mul_f32_e32 v11, v11, v102
	v_mul_f32_e32 v12, v12, v103
	v_med3_f32 v2, v11, s7, v228
	v_med3_f32 v8, v12, s7, v228
	v_cvt_pk_fp8_f32 v7, v2, v8 op_sel:[0,0,1]
	s_mov_b32 s0, 0x18000
	v_add_co_u32_e32 v8, vcc, s0, v4
	v_mul_f32_e32 v2, 0xbfb8aa3b, v96
	s_nop 0
	v_addc_co_u32_e32 v9, vcc, 0, v5, vcc
	global_store_dwordx2 v[8:9], v[6:7], off
	v_mul_f32_e32 v6, 0xbfb8aa3b, v97
	v_exp_f32_e32 v2, v2
	v_exp_f32_e32 v6, v6
	v_mul_f32_e32 v7, 0xbfb8aa3b, v98
	v_mul_f32_e32 v8, 0xbfb8aa3b, v99
	v_add_f32_e32 v2, 1.0, v2
	v_add_f32_e32 v6, 1.0, v6
	v_exp_f32_e32 v7, v7
	v_exp_f32_e32 v8, v8
	v_mul_f32_e32 v9, 0xbfb8aa3b, v88
	v_mul_f32_e32 v10, 0xbfb8aa3b, v89
	v_rcp_f32_e32 v2, v2
	v_rcp_f32_e32 v6, v6
	v_exp_f32_e32 v9, v9
	v_exp_f32_e32 v10, v10
	v_add_f32_e32 v7, 1.0, v7
	v_add_f32_e32 v8, 1.0, v8
	v_mul_f32_e32 v11, 0xbfb8aa3b, v90
	v_mul_f32_e32 v12, 0xbfb8aa3b, v91
	v_mul_f32_e32 v2, v96, v2
	v_mul_f32_e32 v6, v97, v6
	v_rcp_f32_e32 v7, v7
	v_rcp_f32_e32 v8, v8
	v_add_f32_e32 v9, 1.0, v9
	v_add_f32_e32 v10, 1.0, v10
	v_exp_f32_e32 v11, v11
	v_exp_f32_e32 v12, v12
	v_mul_f32_e32 v2, v2, v92
	v_mul_f32_e32 v6, v6, v93
	v_rcp_f32_e32 v9, v9
	v_rcp_f32_e32 v10, v10
	v_med3_f32 v2, v2, s7, v228
	v_med3_f32 v13, v6, s7, v228
	v_mov_b32_e32 v6, v3
	v_cvt_pk_fp8_f32 v6, v2, v13
	v_mul_f32_e32 v7, v98, v7
	v_mul_f32_e32 v8, v99, v8
	v_add_f32_e32 v11, 1.0, v11
	v_add_f32_e32 v12, 1.0, v12
	v_mul_f32_e32 v7, v7, v94
	v_mul_f32_e32 v8, v8, v95
	v_mul_f32_e32 v9, v88, v9
	v_mul_f32_e32 v10, v89, v10
	v_rcp_f32_e32 v11, v11
	v_rcp_f32_e32 v12, v12
	v_mul_f32_e32 v9, v9, v84
	v_mul_f32_e32 v10, v10, v85
	v_med3_f32 v2, v7, s7, v228
	v_med3_f32 v7, v8, s7, v228
	v_cvt_pk_fp8_f32 v6, v2, v7 op_sel:[0,0,1]
	v_med3_f32 v2, v9, s7, v228
	v_med3_f32 v8, v10, s7, v228
	v_mov_b32_e32 v7, v3
	v_cvt_pk_fp8_f32 v7, v2, v8
	v_mul_f32_e32 v11, v90, v11
	v_mul_f32_e32 v12, v91, v12
	v_mul_f32_e32 v11, v11, v86
	v_mul_f32_e32 v12, v12, v87
	v_med3_f32 v2, v11, s7, v228
	v_med3_f32 v8, v12, s7, v228
	v_cvt_pk_fp8_f32 v7, v2, v8 op_sel:[0,0,1]
	v_add_co_u32_e32 v8, vcc, s16, v4
	v_mul_f32_e32 v2, 0xbfb8aa3b, v80
	s_nop 0
	v_addc_co_u32_e32 v9, vcc, 0, v5, vcc
	global_store_dwordx2 v[8:9], v[6:7], off
	v_mul_f32_e32 v6, 0xbfb8aa3b, v81
	v_exp_f32_e32 v2, v2
	v_exp_f32_e32 v6, v6
	v_mul_f32_e32 v7, 0xbfb8aa3b, v82
	v_mul_f32_e32 v8, 0xbfb8aa3b, v83
	v_add_f32_e32 v2, 1.0, v2
	v_add_f32_e32 v6, 1.0, v6
	v_exp_f32_e32 v7, v7
	v_exp_f32_e32 v8, v8
	v_mul_f32_e32 v9, 0xbfb8aa3b, v72
	v_mul_f32_e32 v10, 0xbfb8aa3b, v73
	v_rcp_f32_e32 v2, v2
	v_rcp_f32_e32 v6, v6
	v_exp_f32_e32 v9, v9
	v_exp_f32_e32 v10, v10
	v_add_f32_e32 v7, 1.0, v7
	v_add_f32_e32 v8, 1.0, v8
	v_mul_f32_e32 v11, 0xbfb8aa3b, v74
	v_mul_f32_e32 v12, 0xbfb8aa3b, v75
	v_mul_f32_e32 v2, v80, v2
	v_mul_f32_e32 v6, v81, v6
	v_rcp_f32_e32 v7, v7
	v_rcp_f32_e32 v8, v8
	v_add_f32_e32 v9, 1.0, v9
	v_add_f32_e32 v10, 1.0, v10
	v_exp_f32_e32 v11, v11
	v_exp_f32_e32 v12, v12
	v_mul_f32_e32 v2, v2, v76
	v_mul_f32_e32 v6, v6, v77
	v_rcp_f32_e32 v9, v9
	v_rcp_f32_e32 v10, v10
	v_med3_f32 v2, v2, s7, v228
	v_med3_f32 v13, v6, s7, v228
	v_mov_b32_e32 v6, v3
	v_cvt_pk_fp8_f32 v6, v2, v13
	v_mul_f32_e32 v7, v82, v7
	v_mul_f32_e32 v8, v83, v8
	v_add_f32_e32 v11, 1.0, v11
	v_add_f32_e32 v12, 1.0, v12
	v_mul_f32_e32 v7, v7, v78
	v_mul_f32_e32 v8, v8, v79
	v_mul_f32_e32 v9, v72, v9
	v_mul_f32_e32 v10, v73, v10
	v_rcp_f32_e32 v11, v11
	v_rcp_f32_e32 v12, v12
	v_mul_f32_e32 v9, v9, v68
	v_mul_f32_e32 v10, v10, v69
	v_med3_f32 v2, v7, s7, v228
	v_med3_f32 v7, v8, s7, v228
	v_cvt_pk_fp8_f32 v6, v2, v7 op_sel:[0,0,1]
	v_med3_f32 v2, v9, s7, v228
	v_med3_f32 v8, v10, s7, v228
	v_mov_b32_e32 v7, v3
	v_cvt_pk_fp8_f32 v7, v2, v8
	v_mul_f32_e32 v11, v74, v11
	v_mul_f32_e32 v12, v75, v12
	v_mul_f32_e32 v11, v11, v70
	v_mul_f32_e32 v12, v12, v71
	v_med3_f32 v2, v11, s7, v228
	v_med3_f32 v8, v12, s7, v228
	v_cvt_pk_fp8_f32 v7, v2, v8 op_sel:[0,0,1]
	s_mov_b32 s0, 0x48000
	v_add_co_u32_e32 v8, vcc, s0, v4
	v_mul_f32_e32 v2, 0xbfb8aa3b, v60
	s_nop 0
	v_addc_co_u32_e32 v9, vcc, 0, v5, vcc
	global_store_dwordx2 v[8:9], v[6:7], off
	v_mul_f32_e32 v6, 0xbfb8aa3b, v61
	v_exp_f32_e32 v2, v2
	v_exp_f32_e32 v6, v6
	v_mul_f32_e32 v7, 0xbfb8aa3b, v62
	v_mul_f32_e32 v8, 0xbfb8aa3b, v63
	v_add_f32_e32 v2, 1.0, v2
	v_add_f32_e32 v6, 1.0, v6
	v_exp_f32_e32 v7, v7
	v_exp_f32_e32 v8, v8
	v_mul_f32_e32 v9, 0xbfb8aa3b, v52
	v_mul_f32_e32 v10, 0xbfb8aa3b, v53
	v_rcp_f32_e32 v2, v2
	v_rcp_f32_e32 v6, v6
	v_exp_f32_e32 v9, v9
	v_exp_f32_e32 v10, v10
	v_add_f32_e32 v7, 1.0, v7
	v_add_f32_e32 v8, 1.0, v8
	v_mul_f32_e32 v11, 0xbfb8aa3b, v54
	v_mul_f32_e32 v12, 0xbfb8aa3b, v55
	v_mul_f32_e32 v2, v60, v2
	v_mul_f32_e32 v6, v61, v6
	v_rcp_f32_e32 v7, v7
	v_rcp_f32_e32 v8, v8
	v_add_f32_e32 v9, 1.0, v9
	v_add_f32_e32 v10, 1.0, v10
	v_exp_f32_e32 v11, v11
	v_exp_f32_e32 v12, v12
	v_mul_f32_e32 v2, v2, v64
	v_mul_f32_e32 v6, v6, v65
	v_rcp_f32_e32 v9, v9
	v_rcp_f32_e32 v10, v10
	v_med3_f32 v2, v2, s7, v228
	v_med3_f32 v13, v6, s7, v228
	v_mov_b32_e32 v6, v3
	v_cvt_pk_fp8_f32 v6, v2, v13
	v_mul_f32_e32 v7, v62, v7
	v_mul_f32_e32 v8, v63, v8
	v_add_f32_e32 v11, 1.0, v11
	v_add_f32_e32 v12, 1.0, v12
	v_mul_f32_e32 v7, v7, v66
	v_mul_f32_e32 v8, v8, v67
	v_mul_f32_e32 v9, v52, v9
	v_mul_f32_e32 v10, v53, v10
	v_rcp_f32_e32 v11, v11
	v_rcp_f32_e32 v12, v12
	v_mul_f32_e32 v9, v9, v56
	v_mul_f32_e32 v10, v10, v57
	v_med3_f32 v2, v7, s7, v228
	v_med3_f32 v7, v8, s7, v228
	v_cvt_pk_fp8_f32 v6, v2, v7 op_sel:[0,0,1]
	v_med3_f32 v2, v9, s7, v228
	v_med3_f32 v8, v10, s7, v228
	v_mov_b32_e32 v7, v3
	v_cvt_pk_fp8_f32 v7, v2, v8
	v_mul_f32_e32 v11, v54, v11
	v_mul_f32_e32 v12, v55, v12
	v_mul_f32_e32 v11, v11, v58
	v_mul_f32_e32 v12, v12, v59
	v_med3_f32 v2, v11, s7, v228
	v_med3_f32 v8, v12, s7, v228
	v_cvt_pk_fp8_f32 v7, v2, v8 op_sel:[0,0,1]
	s_mov_b32 s0, 0x50000
	v_add_co_u32_e32 v8, vcc, s0, v4
	v_mul_f32_e32 v2, 0xbfb8aa3b, v44
	s_nop 0
	v_addc_co_u32_e32 v9, vcc, 0, v5, vcc
	global_store_dwordx2 v[8:9], v[6:7], off
	v_mul_f32_e32 v6, 0xbfb8aa3b, v45
	v_exp_f32_e32 v2, v2
	v_exp_f32_e32 v6, v6
	v_mul_f32_e32 v7, 0xbfb8aa3b, v46
	v_mul_f32_e32 v8, 0xbfb8aa3b, v47
	v_add_f32_e32 v2, 1.0, v2
	v_add_f32_e32 v6, 1.0, v6
	v_exp_f32_e32 v7, v7
	v_exp_f32_e32 v8, v8
	v_mul_f32_e32 v9, 0xbfb8aa3b, v36
	v_mul_f32_e32 v10, 0xbfb8aa3b, v37
	v_rcp_f32_e32 v2, v2
	v_rcp_f32_e32 v6, v6
	v_exp_f32_e32 v9, v9
	v_exp_f32_e32 v10, v10
	v_add_f32_e32 v7, 1.0, v7
	v_add_f32_e32 v8, 1.0, v8
	v_mul_f32_e32 v11, 0xbfb8aa3b, v38
	v_mul_f32_e32 v12, 0xbfb8aa3b, v39
	v_mul_f32_e32 v2, v44, v2
	v_mul_f32_e32 v6, v45, v6
	v_rcp_f32_e32 v7, v7
	v_rcp_f32_e32 v8, v8
	v_add_f32_e32 v9, 1.0, v9
	v_add_f32_e32 v10, 1.0, v10
	v_exp_f32_e32 v11, v11
	v_exp_f32_e32 v12, v12
	v_mul_f32_e32 v2, v2, v48
	v_mul_f32_e32 v6, v6, v49
	v_rcp_f32_e32 v9, v9
	v_rcp_f32_e32 v10, v10
	v_med3_f32 v2, v2, s7, v228
	v_med3_f32 v13, v6, s7, v228
	v_mov_b32_e32 v6, v3
	v_cvt_pk_fp8_f32 v6, v2, v13
	v_mul_f32_e32 v7, v46, v7
	v_mul_f32_e32 v8, v47, v8
	v_add_f32_e32 v11, 1.0, v11
	v_add_f32_e32 v12, 1.0, v12
	v_mul_f32_e32 v7, v7, v50
	v_mul_f32_e32 v8, v8, v51
	v_mul_f32_e32 v9, v36, v9
	v_mul_f32_e32 v10, v37, v10
	v_rcp_f32_e32 v11, v11
	v_rcp_f32_e32 v12, v12
	v_mul_f32_e32 v9, v9, v40
	v_mul_f32_e32 v10, v10, v41
	v_med3_f32 v2, v7, s7, v228
	v_med3_f32 v7, v8, s7, v228
	v_cvt_pk_fp8_f32 v6, v2, v7 op_sel:[0,0,1]
	v_med3_f32 v2, v9, s7, v228
	v_med3_f32 v8, v10, s7, v228
	v_mov_b32_e32 v7, v3
	v_cvt_pk_fp8_f32 v7, v2, v8
	v_mul_f32_e32 v11, v38, v11
	v_mul_f32_e32 v12, v39, v12
	v_mul_f32_e32 v11, v11, v42
	v_mul_f32_e32 v12, v12, v43
	v_med3_f32 v2, v11, s7, v228
	v_med3_f32 v8, v12, s7, v228
	v_cvt_pk_fp8_f32 v7, v2, v8 op_sel:[0,0,1]
	v_add_co_u32_e32 v4, vcc, 0x58000, v4
	v_mov_b32_e32 v176, v204
	s_nop 0
	v_addc_co_u32_e32 v5, vcc, 0, v5, vcc
	s_and_b64 vcc, exec, s[38:39]
	v_mov_b32_e32 v178, v205
	v_mov_b32_e32 v180, v203
	v_mov_b32_e32 v184, v202
	s_mov_b32 s3, s44
	s_mov_b32 s48, s42
	s_mov_b64 s[50:51], s[46:47]
	global_store_dwordx2 v[4:5], v[6:7], off
	s_lshl_b32 s72, s32, 8
	s_add_i32 s72, s72, s2
	s_add_i32 s32, s32, 2
	s_cmpk_ge_i32 s72, 7136
	s_cbranch_scc1 .Lcvd_p2_end
	v_readlane_b32 s78, v255, 42
	v_readlane_b32 s79, v255, 43
	s_addk_i32 s72, 1056
	s_lshr_b32 s80, s72, 9
	s_lshl_b32 s80, s80, 21
	s_and_b32 s81, s72, 15
	s_lshl_b32 s81, s81, 17
	s_add_i32 s80, s80, s81
	s_bfe_u32 s81, s72, 0x50004
	s_lshl_b32 s81, s81, 6
	s_add_i32 s80, s80, s81
	v_and_b32_e32 v150, 63, v0
	v_lshlrev_b32_e32 v150, 11, v150
	v_add_u32_e32 v156, s80, v150
	s_waitcnt vmcnt(6)
	v_mul_f32_e32 v134, 0x42800000, v134
	v_mul_f32_e32 v135, 0x42800000, v135
	v_mul_f32_e32 v136, 0x42800000, v136
	v_mul_f32_e32 v137, 0x42800000, v137
	v_mul_f32_e32 v138, 0x42800000, v138
	v_mul_f32_e32 v139, 0x42800000, v139
	v_mul_f32_e32 v140, 0x42800000, v140
	v_mul_f32_e32 v141, 0x42800000, v141
	v_med3_f32 v134, v134, s7, v228
	v_med3_f32 v135, v135, s7, v228
	v_med3_f32 v136, v136, s7, v228
	v_med3_f32 v137, v137, s7, v228
	v_med3_f32 v138, v138, s7, v228
	v_med3_f32 v139, v139, s7, v228
	v_med3_f32 v140, v140, s7, v228
	v_med3_f32 v141, v141, s7, v228
	v_cvt_pk_fp8_f32 v152, v134, v135
	v_cvt_pk_fp8_f32 v153, v138, v139
	v_cvt_pk_fp8_f32 v152, v136, v137 op_sel:[0,0,1]
	v_cvt_pk_fp8_f32 v153, v140, v141 op_sel:[0,0,1]
	s_nop 1
	global_store_dwordx2 v156, v[152:153], s[78:79]
	s_cmpk_ge_i32 s72, 7936
	s_cbranch_scc1 .Lcvd_p2_end
	s_addk_i32 s72, 0x100
	s_lshr_b32 s80, s72, 9
	s_lshl_b32 s80, s80, 21
	s_and_b32 s81, s72, 15
	s_lshl_b32 s81, s81, 17
	s_add_i32 s80, s80, s81
	s_bfe_u32 s81, s72, 0x50004
	s_lshl_b32 s81, s81, 6
	s_add_i32 s80, s80, s81
	v_add_u32_e32 v157, s80, v150
	v_mul_f32_e32 v142, 0x42800000, v142
	v_mul_f32_e32 v143, 0x42800000, v143
	v_mul_f32_e32 v144, 0x42800000, v144
	v_mul_f32_e32 v145, 0x42800000, v145
	v_mul_f32_e32 v146, 0x42800000, v146
	v_mul_f32_e32 v147, 0x42800000, v147
	v_mul_f32_e32 v148, 0x42800000, v148
	v_mul_f32_e32 v149, 0x42800000, v149
	v_med3_f32 v142, v142, s7, v228
	v_med3_f32 v143, v143, s7, v228
	v_med3_f32 v144, v144, s7, v228
	v_med3_f32 v145, v145, s7, v228
	v_med3_f32 v146, v146, s7, v228
	v_med3_f32 v147, v147, s7, v228
	v_med3_f32 v148, v148, s7, v228
	v_med3_f32 v149, v149, s7, v228
	v_cvt_pk_fp8_f32 v154, v142, v143
	v_cvt_pk_fp8_f32 v155, v146, v147
	v_cvt_pk_fp8_f32 v154, v144, v145 op_sel:[0,0,1]
	v_cvt_pk_fp8_f32 v155, v148, v149 op_sel:[0,0,1]
	s_nop 1
	global_store_dwordx2 v157, v[154:155], s[78:79]
.Lcvd_p2_end:
	s_cbranch_vccnz .LBB0_1919
